# MLA loop: fully masked wave-tiles on the diagonal skip QK/softmax/PV (state unchanged), on top of counted LDS waits in all P.V sections
# speedup vs baseline: 1.0073x; 1.0008x over previous
; #define FA_SBAR() __builtin_amdgcn_sched_barrier(0)
; __device__ __forceinline__ int crow(int r, int hi) { return (r & 3) + 8 * (r >> 2) + 4 * hi; }
; #define MLA_SLOAD(k0) do { const char* kvp = KVu + (size_t)(k0) * 4096; const char* zp = Zu + (size_t)(k0) * (NABC * 2); \
;             ks0 = *(const v4u*)(kvp + kvoff); vs0 = *(const v4u*)(kvp + kvoff + 256); ks1 = *(const v4u*)(kvp + 32 * 4096 + kvoff); vs1 = *(const v4u*)(kvp + 32 * 4096 + kvoff + 256); \
;             krr = *(const v4u*)(zp + zoff); } while (0)
; __device__ __forceinline__ void mla_attn_phase(LAS unsigned char* lds, const bf16* Q, const bf16* KV, const bf16* Z, bf16* Oabc, const float* ropec, const float* ropes, int vcu, int G, int tid) {
;     ...
;             for (int t = 0; t < nt; ++t) {
;                 const int buf = t & 1;
;                 if (t + 1 < nt) MLA_SLOAD((t + 1) * 64);
;                 FA_SBAR();
;                 const int tt = t - 4 * qb;
;                 {
;     ...
;                     if (tt >= 0) { const int rrel = 32 * wid + r32 - 64 * tt;
; #pragma unroll
;                         for (int r = 0; r < 16; ++r) { const int kk = crow(r, hi); if (kk > rrel) p0[r] = -1e30f; if (32 + kk > rrel) p1[r] = -1e30f; } }
.LBB0_1127:
	s_add_i32 s6, s50, -1
	s_and_b32 s51, s6, 1
	s_add_i32 s7, s6, s45
	s_cmp_lt_i32 s7, 1
	s_cbranch_scc1 .Lmla_noskip
	s_lshl_b32 s7, s7, 7
	v_readlane_b32 s98, v252, 37
	s_nop 3
	s_cmp_lt_u32 s98, s7
	s_cbranch_scc0 .Lmla_noskip
	v_mov_b32_e32 v6, 0
	v_mov_b32_e32 v7, 0
	v_mov_b32_e32 v0, 1.0
	s_andn2_b64 vcc, exec, s[14:15]
	s_branch .Lmla_skip
; #define LAS __attribute__((address_space(3)))
; #define FA_SBAR() __builtin_amdgcn_sched_barrier(0)
; __device__ __forceinline__ int crow(int r, int hi) { return (r & 3) + 8 * (r >> 2) + 4 * hi; }
; __device__ __forceinline__ void mla_attn_phase(LAS unsigned char* lds, const bf16* Q, const bf16* KV, const bf16* Z, bf16* Oabc, const float* ropec, const float* ropes, int vcu, int G, int tid) {
;     ...
;                     const LAS unsigned char* Ks = K_lds + buf * SHM_K;
;                     bf16x8 kf[2][4], qx[2][2];
;     ...
;                     MLA_KREAD(0);
; #pragma unroll
;                     for (int g = 0; g < 6; ++g) {
;                         if (g + 1 < 6) MLA_KREAD(g + 1);
;                         FA_SBAR();
; #pragma unroll
;                         for (int e = 0; e < 2; ++e) { const int d0 = 2 * g + e; const bf16x8 qv = (d0 < 8) ? qr[d0 < 8 ? d0 : 0] : qx[g & 1][e];
;                             p0 = __builtin_amdgcn_mfma_f32_32x32x16_bf16(kf[g & 1][2 * e], qv, p0, 0, 0, 0);
;                             p1 = __builtin_amdgcn_mfma_f32_32x32x16_bf16(kf[g & 1][2 * e + 1], qv, p1, 0, 0, 0); }
;                         FA_SBAR(); }
;     ...
;                     if (tt >= 0) { const int rrel = 32 * wid + r32 - 64 * tt;
; #pragma unroll
;                         for (int r = 0; r < 16; ++r) { const int kk = crow(r, hi); if (kk > rrel) p0[r] = -1e30f; if (32 + kk > rrel) p1[r] = -1e30f; } }
.Lmla_noskip:
	s_mul_i32 s7, s51, 0x6000
	s_add_i32 s7, s7, 0
	v_add_u32_e32 v0, s7, v200
	v_add_u32_e32 v14, s7, v201
	v_add_u32_e32 v15, s7, v202
	v_add_u32_e32 v218, s7, v203
	ds_read_b128 v[2:5], v0
	ds_read_b128 v[6:9], v0 offset:12288
	ds_read_b128 v[10:13], v14
	ds_read_b128 v[236:239], v14 offset:12288
	ds_read_b128 v[240:243], v15
	ds_read_b128 v[244:247], v15 offset:12288
	ds_read_b128 v[248:251], v218
	ds_read_b128 v[182:185], v218 offset:12288
	s_waitcnt lgkmcnt(7)
	v_mfma_f32_32x32x16_bf16 v[96:111], v[2:5], v[112:115], 0
	s_waitcnt lgkmcnt(6)
	v_mfma_f32_32x32x16_bf16 v[80:95], v[6:9], v[112:115], 0
	s_waitcnt lgkmcnt(5)
	v_mfma_f32_32x32x16_bf16 v[96:111], v[10:13], v[116:119], v[96:111]
	s_waitcnt lgkmcnt(4)
	v_mfma_f32_32x32x16_bf16 v[80:95], v[236:239], v[116:119], v[80:95]
	ds_read_b128 v[2:5], v0 offset:128
	ds_read_b128 v[6:9], v0 offset:12416
	ds_read_b128 v[10:13], v14 offset:128
	ds_read_b128 v[236:239], v14 offset:12416
	s_waitcnt lgkmcnt(7)
	v_mfma_f32_32x32x16_bf16 v[96:111], v[240:243], v[120:123], v[96:111]
	s_waitcnt lgkmcnt(6)
	v_mfma_f32_32x32x16_bf16 v[80:95], v[244:247], v[120:123], v[80:95]
	s_waitcnt lgkmcnt(5)
	v_mfma_f32_32x32x16_bf16 v[96:111], v[248:251], v[124:127], v[96:111]
	s_waitcnt lgkmcnt(4)
	v_mfma_f32_32x32x16_bf16 v[80:95], v[182:185], v[124:127], v[80:95]
	ds_read_b128 v[182:185], v15 offset:128
	ds_read_b128 v[240:243], v15 offset:12416
	ds_read_b128 v[244:247], v218 offset:128
	ds_read_b128 v[248:251], v218 offset:12416
	s_waitcnt lgkmcnt(7)
	v_mfma_f32_32x32x16_bf16 v[96:111], v[2:5], v[128:131], v[96:111]
	s_waitcnt lgkmcnt(6)
	v_mfma_f32_32x32x16_bf16 v[80:95], v[6:9], v[128:131], v[80:95]
	s_waitcnt lgkmcnt(5)
	v_mfma_f32_32x32x16_bf16 v[96:111], v[10:13], v[132:135], v[96:111]
	s_waitcnt lgkmcnt(4)
	v_mfma_f32_32x32x16_bf16 v[80:95], v[236:239], v[132:135], v[80:95]
	ds_read_b128 v[2:5], v0 offset:256
	ds_read_b128 v[6:9], v0 offset:12544
	ds_read_b128 v[10:13], v14 offset:256
	ds_read_b128 v[236:239], v14 offset:12544
	ds_read_b128 v[186:189], v214
	ds_read_b128 v[178:181], v214 offset:1024
	s_waitcnt lgkmcnt(9)
	v_mfma_f32_32x32x16_bf16 v[96:111], v[182:185], v[136:139], v[96:111]
	s_waitcnt lgkmcnt(8)
	v_mfma_f32_32x32x16_bf16 v[80:95], v[240:243], v[136:139], v[80:95]
	s_waitcnt lgkmcnt(7)
	v_mfma_f32_32x32x16_bf16 v[96:111], v[244:247], v[140:143], v[96:111]
	s_waitcnt lgkmcnt(6)
	v_mfma_f32_32x32x16_bf16 v[80:95], v[248:251], v[140:143], v[80:95]
	ds_read_b128 v[182:185], v15 offset:256
	ds_read_b128 v[240:243], v15 offset:12544
	ds_read_b128 v[244:247], v218 offset:256
	ds_read_b128 v[248:251], v218 offset:12544
	ds_read_b128 v[226:229], v214 offset:2048
	ds_read_b128 v[218:221], v214 offset:3072
	s_waitcnt lgkmcnt(7)
	v_mfma_f32_32x32x16_bf16 v[96:111], v[2:5], v[186:189], v[96:111]
	v_mfma_f32_32x32x16_bf16 v[80:95], v[6:9], v[186:189], v[80:95]
	s_waitcnt lgkmcnt(6)
	v_mfma_f32_32x32x16_bf16 v[96:111], v[10:13], v[178:181], v[96:111]
	v_mfma_f32_32x32x16_bf16 v[80:95], v[236:239], v[178:181], v[80:95]
	s_waitcnt lgkmcnt(1)
	v_mfma_f32_32x32x16_bf16 v[96:111], v[182:185], v[226:229], v[96:111]
	v_mfma_f32_32x32x16_bf16 v[80:95], v[240:243], v[226:229], v[80:95]
	s_waitcnt lgkmcnt(0)
	v_mfma_f32_32x32x16_bf16 v[96:111], v[244:247], v[218:221], v[96:111]
	v_mfma_f32_32x32x16_bf16 v[80:95], v[248:251], v[218:221], v[80:95]
	s_add_i32 s6, s6, s45
	s_cmp_lt_i32 s6, 0
	s_cbranch_scc1 .LBB0_1129
	v_or_b32_e32 v0, 32, v211
	v_cmp_le_i32_e32 vcc, v0, v215
	v_or_b32_e32 v0, 33, v211
	s_nop 5
	v_cndmask_b32_e32 v80, v231, v80, vcc
	v_cmp_lt_i32_e32 vcc, v211, v215
	s_nop 1
	v_cndmask_b32_e32 v97, v231, v97, vcc
	v_cmp_le_i32_e32 vcc, v211, v215
	s_nop 1
	v_cndmask_b32_e32 v96, v231, v96, vcc
	v_cmp_le_i32_e32 vcc, v0, v215
	v_or_b32_e32 v0, 2, v211
	s_nop 0
	v_cndmask_b32_e32 v81, v231, v81, vcc
	v_cmp_le_i32_e32 vcc, v0, v215
	v_or_b32_e32 v0, 34, v211
	s_nop 0
	v_cndmask_b32_e32 v98, v231, v98, vcc
	v_cmp_le_i32_e32 vcc, v0, v215
	v_or_b32_e32 v0, 3, v211
	s_nop 0
	v_cndmask_b32_e32 v82, v231, v82, vcc
	v_cmp_le_i32_e32 vcc, v0, v215
	v_or_b32_e32 v0, 35, v211
	s_nop 0
	v_cndmask_b32_e32 v99, v231, v99, vcc
	v_cmp_le_i32_e32 vcc, v0, v215
	v_or_b32_e32 v0, 8, v211
	s_nop 0
	v_cndmask_b32_e32 v83, v231, v83, vcc
	v_cmp_le_i32_e32 vcc, v0, v215
	v_or_b32_e32 v0, 40, v211
	s_nop 0
	v_cndmask_b32_e32 v100, v231, v100, vcc
	v_cmp_le_i32_e32 vcc, v0, v215
	v_or_b32_e32 v0, 9, v211
	s_nop 0
	v_cndmask_b32_e32 v84, v231, v84, vcc
	v_cmp_le_i32_e32 vcc, v0, v215
	v_or_b32_e32 v0, 41, v211
	s_nop 0
	v_cndmask_b32_e32 v101, v231, v101, vcc
	v_cmp_le_i32_e32 vcc, v0, v215
	v_or_b32_e32 v0, 10, v211
	s_nop 0
	v_cndmask_b32_e32 v85, v231, v85, vcc
	v_cmp_le_i32_e32 vcc, v0, v215
	v_or_b32_e32 v0, 42, v211
	s_nop 0
	v_cndmask_b32_e32 v102, v231, v102, vcc
	v_cmp_le_i32_e32 vcc, v0, v215
	v_or_b32_e32 v0, 11, v211
	s_nop 0
	v_cndmask_b32_e32 v86, v231, v86, vcc
	v_cmp_le_i32_e32 vcc, v0, v215
	v_or_b32_e32 v0, 43, v211
	s_nop 0
	v_cndmask_b32_e32 v103, v231, v103, vcc
	v_cmp_le_i32_e32 vcc, v0, v215
	v_or_b32_e32 v0, 16, v211
	s_nop 0
	v_cndmask_b32_e32 v87, v231, v87, vcc
	v_cmp_le_i32_e32 vcc, v0, v215
	v_or_b32_e32 v0, 48, v211
	s_nop 0
	v_cndmask_b32_e32 v104, v231, v104, vcc
	v_cmp_le_i32_e32 vcc, v0, v215
	v_or_b32_e32 v0, 17, v211
	s_nop 0
	v_cndmask_b32_e32 v88, v231, v88, vcc
	v_cmp_le_i32_e32 vcc, v0, v215
	v_or_b32_e32 v0, 49, v211
	s_nop 0
	v_cndmask_b32_e32 v105, v231, v105, vcc
	v_cmp_le_i32_e32 vcc, v0, v215
	v_or_b32_e32 v0, 18, v211
	s_nop 0
	v_cndmask_b32_e32 v89, v231, v89, vcc
	v_cmp_le_i32_e32 vcc, v0, v215
	v_or_b32_e32 v0, 50, v211
	s_nop 0
	v_cndmask_b32_e32 v106, v231, v106, vcc
	v_cmp_le_i32_e32 vcc, v0, v215
	v_or_b32_e32 v0, 19, v211
	s_nop 0
	v_cndmask_b32_e32 v90, v231, v90, vcc
	v_cmp_le_i32_e32 vcc, v0, v215
	v_or_b32_e32 v0, 51, v211
	s_nop 0
	v_cndmask_b32_e32 v107, v231, v107, vcc
	v_cmp_le_i32_e32 vcc, v0, v215
	v_or_b32_e32 v0, 24, v211
	s_nop 0
	v_cndmask_b32_e32 v91, v231, v91, vcc
	v_cmp_le_i32_e32 vcc, v0, v215
	v_or_b32_e32 v0, 56, v211
	s_nop 0
	v_cndmask_b32_e32 v108, v231, v108, vcc
	v_cmp_le_i32_e32 vcc, v0, v215
	v_or_b32_e32 v0, 25, v211
	s_nop 0
	v_cndmask_b32_e32 v92, v231, v92, vcc
	v_cmp_le_i32_e32 vcc, v0, v215
	v_or_b32_e32 v0, 57, v211
	s_nop 0
	v_cndmask_b32_e32 v109, v231, v109, vcc
	v_cmp_le_i32_e32 vcc, v0, v215
	v_or_b32_e32 v0, 26, v211
	s_nop 0
	v_cndmask_b32_e32 v93, v231, v93, vcc
	v_cmp_le_i32_e32 vcc, v0, v215
	v_or_b32_e32 v0, 58, v211
	s_nop 0
	v_cndmask_b32_e32 v110, v231, v110, vcc
	v_cmp_le_i32_e32 vcc, v0, v215
	v_or_b32_e32 v0, 27, v211
	s_nop 0
	v_cndmask_b32_e32 v94, v231, v94, vcc
	v_cmp_le_i32_e32 vcc, v0, v215
	v_or_b32_e32 v0, 59, v211
	s_nop 0
	v_cndmask_b32_e32 v111, v231, v111, vcc
	v_cmp_le_i32_e32 vcc, v0, v215
	s_nop 1
	v_cndmask_b32_e32 v95, v231, v95, vcc

; #define MLA_SWRITE(bb) do { *(LAS v4u*)(V_lds + (bb) * SHM_V + vst0) = vs0; *(LAS v4u*)(V_lds + (bb) * SHM_V + vst0 + 8192) = vs1; \
;             *(LAS v4u*)(K_lds + (bb) * SHM_K + kst0) = ks0; *(LAS v4u*)(K_lds + (bb) * SHM_K + kst0 + 32 * 384) = ks1; \
;             *(LAS v4u*)(K_lds + (bb) * SHM_K + kst2) = krr; } while (0)
; __device__ __forceinline__ void mla_attn_phase(LAS unsigned char* lds, const bf16* Q, const bf16* KV, const bf16* Z, bf16* Oabc, const float* ropec, const float* ropes, int vcu, int G, int tid) {
;     ...
;                 if (t + 1 < nt) MLA_SWRITE(buf ^ 1);
.Lmla_skip:
	s_cbranch_vccnz .LBB0_1135
	s_xor_b32 s6, s51, 1
	v_lshl_add_u32 v2, s6, 14, v210
	s_mulk_i32 s6, 0x6000
	s_add_i32 s6, s6, 0
	s_waitcnt vmcnt(3)
	ds_write_b128 v2, v[148:151] offset:49152
	s_waitcnt vmcnt(1)
	ds_write_b128 v2, v[156:159] offset:57344
	v_add_u32_e32 v2, s6, v204
	ds_write_b128 v2, v[144:147]
	ds_write_b128 v2, v[152:155] offset:12288
	v_add_u32_e32 v2, s6, v199
	s_waitcnt vmcnt(0)
	ds_write_b128 v2, v[160:163]
